# passL: static s_setprio 1 for the later-dispatched half of the grid (blocks >= 512)
# speedup vs baseline: 1.0069x; 1.0069x over previous
.LBB7_8:
	s_load_dwordx2 s[12:13], s[0:1], 0x68
	s_lshl_b32 s17, s6, 5
	s_lshl_b32 s18, s10, 5
	s_sub_i32 s4, s18, s17
	s_ashr_i32 s16, s4, 5
	s_cmp_lt_i32 s16, 1
	v_and_b32_e32 v1, 63, v0
	s_cbranch_scc1 .LBB7_13
	s_load_dwordx8 s[4:11], s[0:1], 0x0
	s_load_dwordx2 s[14:15], s[0:1], 0x20
	v_and_b32_e32 v54, 7, v1
	v_lshlrev_b32_e32 v54, 4, v54
	v_lshrrev_b32_e32 v56, 3, v1
	v_lshlrev_b32_e32 v55, 1, v54
	ds_read_b128 v[2:5], v55 offset:18432
	ds_read_b128 v[6:9], v55 offset:18448
	ds_read_b128 v[10:13], v55 offset:18944
	ds_read_b128 v[14:17], v55 offset:18960
	ds_read_b128 v[18:21], v55 offset:18688
	ds_read_b128 v[22:25], v55 offset:18704
	s_mul_i32 s21, s3, 0x1200
	s_add_i32 s21, s21, 0x4b00
	v_mul_u32_u24_e32 v58, 0x240, v56
	v_add3_u32 v58, v58, v54, s21
	v_and_b32_e32 v59, 31, v1
	v_mul_u32_u24_e32 v59, 0x90, v59
	v_lshrrev_b32_e32 v57, 5, v1
	v_lshlrev_b32_e32 v57, 6, v57
	v_add3_u32 v59, v59, v57, s21
	v_lshlrev_b32_e32 v56, 4, v56
	v_lshlrev_b32_e32 v57, 4, v1
	v_mov_b32_e32 v50, 0
	v_mov_b32_e32 v51, 0
	v_mov_b32_e32 v52, 0
	v_mov_b32_e32 v53, 0
	s_lshl_b32 s20, s17, 2
	s_add_i32 s20, s20, 0x100
	s_mov_b32 s22, 0x3d0880
	s_mov_b32 s52, 0xffff0000
	s_waitcnt vmcnt(0) lgkmcnt(0)
	v_mov_b32_e32 v26, v104
	v_mov_b32_e32 v27, v105
	v_mov_b32_e32 v28, v106
	v_mov_b32_e32 v29, v107
	v_mov_b32_e32 v30, v108
	v_mov_b32_e32 v31, v109
	v_mov_b32_e32 v32, v110
	v_mov_b32_e32 v33, v111
	v_mov_b32_e32 v38, v112
	v_mov_b32_e32 v39, v113
	v_mov_b32_e32 v40, v114
	v_mov_b32_e32 v41, v115
	v_mov_b32_e32 v34, v100
	v_mov_b32_e32 v35, v101
	v_mov_b32_e32 v36, v102
	v_mov_b32_e32 v37, v103
	s_bitcmp1_b32 s2, 9
	s_cbranch_scc0 .Lpl_nopri
	s_setprio 1
.Lpl_nopri:
.Lpl_loop:
	s_waitcnt vmcnt(3)
	v_lshlrev_b32_e32 v92, 16, v60
	v_and_b32_e32 v93, 0xffff0000, v60
	v_lshlrev_b32_e32 v94, 16, v76
	v_and_b32_e32 v95, 0xffff0000, v76
	v_add_f32_e32 v92, v94, v92
	v_add_f32_e32 v93, v95, v93
	v_fma_f32 v94, v10, v34, v18
	v_fma_f32 v95, v11, v34, v19
	v_fmac_f32_e32 v94, v2, v92
	v_fmac_f32_e32 v95, v3, v93
	v_max_f32_e32 v94, 0, v94
	v_max_f32_e32 v95, 0, v95
	v_cvt_pk_f16_f32 v100, v94, v95
	v_lshlrev_b32_e32 v96, 16, v61
	v_and_b32_e32 v97, 0xffff0000, v61
	v_lshlrev_b32_e32 v98, 16, v77
	v_and_b32_e32 v99, 0xffff0000, v77
	v_add_f32_e32 v96, v98, v96
	v_add_f32_e32 v97, v99, v97
	v_fma_f32 v98, v12, v34, v20
	v_fma_f32 v99, v13, v34, v21
	v_fmac_f32_e32 v98, v4, v96
	v_fmac_f32_e32 v99, v5, v97
	v_max_f32_e32 v98, 0, v98
	v_max_f32_e32 v99, 0, v99
	v_cvt_pk_f16_f32 v101, v98, v99
	v_lshlrev_b32_e32 v92, 16, v62
	v_and_b32_e32 v93, 0xffff0000, v62
	v_lshlrev_b32_e32 v94, 16, v78
	v_and_b32_e32 v95, 0xffff0000, v78
	v_add_f32_e32 v92, v94, v92
	v_add_f32_e32 v93, v95, v93
	v_fma_f32 v94, v14, v34, v22
	v_fma_f32 v95, v15, v34, v23
	v_fmac_f32_e32 v94, v6, v92
	v_fmac_f32_e32 v95, v7, v93
	v_max_f32_e32 v94, 0, v94
	v_max_f32_e32 v95, 0, v95
	v_cvt_pk_f16_f32 v102, v94, v95
	v_lshlrev_b32_e32 v96, 16, v63
	v_and_b32_e32 v97, 0xffff0000, v63
	v_lshlrev_b32_e32 v98, 16, v79
	v_and_b32_e32 v99, 0xffff0000, v79
	v_add_f32_e32 v96, v98, v96
	v_add_f32_e32 v97, v99, v97
	v_fma_f32 v98, v16, v34, v24
	v_fma_f32 v99, v17, v34, v25
	v_fmac_f32_e32 v98, v8, v96
	v_fmac_f32_e32 v99, v9, v97
	v_max_f32_e32 v98, 0, v98
	v_max_f32_e32 v99, 0, v99
	v_cvt_pk_f16_f32 v103, v98, v99
	ds_write_b128 v58, v[100:103]
	v_lshlrev_b32_e32 v92, 16, v64
	v_and_b32_e32 v93, 0xffff0000, v64
	v_lshlrev_b32_e32 v94, 16, v80
	v_and_b32_e32 v95, 0xffff0000, v80
	v_add_f32_e32 v92, v94, v92
	v_add_f32_e32 v93, v95, v93
	v_fma_f32 v94, v10, v35, v18
	v_fma_f32 v95, v11, v35, v19
	v_fmac_f32_e32 v94, v2, v92
	v_fmac_f32_e32 v95, v3, v93
	v_max_f32_e32 v94, 0, v94
	v_max_f32_e32 v95, 0, v95
	v_cvt_pk_f16_f32 v104, v94, v95
	v_lshlrev_b32_e32 v96, 16, v65
	v_and_b32_e32 v97, 0xffff0000, v65
	v_lshlrev_b32_e32 v98, 16, v81
	v_and_b32_e32 v99, 0xffff0000, v81
	v_add_f32_e32 v96, v98, v96
	v_add_f32_e32 v97, v99, v97
	v_fma_f32 v98, v12, v35, v20
	v_fma_f32 v99, v13, v35, v21
	v_fmac_f32_e32 v98, v4, v96
	v_fmac_f32_e32 v99, v5, v97
	v_max_f32_e32 v98, 0, v98
	v_max_f32_e32 v99, 0, v99
	v_cvt_pk_f16_f32 v105, v98, v99
	v_lshlrev_b32_e32 v92, 16, v66
	v_and_b32_e32 v93, 0xffff0000, v66
	v_lshlrev_b32_e32 v94, 16, v82
	v_and_b32_e32 v95, 0xffff0000, v82
	v_add_f32_e32 v92, v94, v92
	v_add_f32_e32 v93, v95, v93
	v_fma_f32 v94, v14, v35, v22
	v_fma_f32 v95, v15, v35, v23
	v_fmac_f32_e32 v94, v6, v92
	v_fmac_f32_e32 v95, v7, v93
	v_max_f32_e32 v94, 0, v94
	v_max_f32_e32 v95, 0, v95
	v_cvt_pk_f16_f32 v106, v94, v95
	v_lshlrev_b32_e32 v96, 16, v67
	v_and_b32_e32 v97, 0xffff0000, v67
	v_lshlrev_b32_e32 v98, 16, v83
	v_and_b32_e32 v99, 0xffff0000, v83
	v_add_f32_e32 v96, v98, v96
	v_add_f32_e32 v97, v99, v97
	v_fma_f32 v98, v16, v35, v24
	v_fma_f32 v99, v17, v35, v25
	v_fmac_f32_e32 v98, v8, v96
	v_fmac_f32_e32 v99, v9, v97
	v_max_f32_e32 v98, 0, v98
	v_max_f32_e32 v99, 0, v99
	v_cvt_pk_f16_f32 v107, v98, v99
	ds_write_b128 v58, v[104:107] offset:144
	v_lshlrev_b32_e32 v92, 16, v68
	v_and_b32_e32 v93, 0xffff0000, v68
	v_lshlrev_b32_e32 v94, 16, v84
	v_and_b32_e32 v95, 0xffff0000, v84
	v_add_f32_e32 v92, v94, v92
	v_add_f32_e32 v93, v95, v93
	v_fma_f32 v94, v10, v36, v18
	v_fma_f32 v95, v11, v36, v19
	v_fmac_f32_e32 v94, v2, v92
	v_fmac_f32_e32 v95, v3, v93
	v_max_f32_e32 v94, 0, v94
	v_max_f32_e32 v95, 0, v95
	v_cvt_pk_f16_f32 v100, v94, v95
	v_lshlrev_b32_e32 v96, 16, v69
	v_and_b32_e32 v97, 0xffff0000, v69
	v_lshlrev_b32_e32 v98, 16, v85
	v_and_b32_e32 v99, 0xffff0000, v85
	v_add_f32_e32 v96, v98, v96
	v_add_f32_e32 v97, v99, v97
	v_fma_f32 v98, v12, v36, v20
	v_fma_f32 v99, v13, v36, v21
	v_fmac_f32_e32 v98, v4, v96
	v_fmac_f32_e32 v99, v5, v97
	v_max_f32_e32 v98, 0, v98
	v_max_f32_e32 v99, 0, v99
	v_cvt_pk_f16_f32 v101, v98, v99
	v_lshlrev_b32_e32 v92, 16, v70
	v_and_b32_e32 v93, 0xffff0000, v70
	v_lshlrev_b32_e32 v94, 16, v86
	v_and_b32_e32 v95, 0xffff0000, v86
	v_add_f32_e32 v92, v94, v92
	v_add_f32_e32 v93, v95, v93
	v_fma_f32 v94, v14, v36, v22
	v_fma_f32 v95, v15, v36, v23
	v_fmac_f32_e32 v94, v6, v92
	v_fmac_f32_e32 v95, v7, v93
	v_max_f32_e32 v94, 0, v94
	v_max_f32_e32 v95, 0, v95
	v_cvt_pk_f16_f32 v102, v94, v95
	v_lshlrev_b32_e32 v96, 16, v71
	v_and_b32_e32 v97, 0xffff0000, v71
	v_lshlrev_b32_e32 v98, 16, v87
	v_and_b32_e32 v99, 0xffff0000, v87
	v_add_f32_e32 v96, v98, v96
	v_add_f32_e32 v97, v99, v97
	v_fma_f32 v98, v16, v36, v24
	v_fma_f32 v99, v17, v36, v25
	v_fmac_f32_e32 v98, v8, v96
	v_fmac_f32_e32 v99, v9, v97
	v_max_f32_e32 v98, 0, v98
	v_max_f32_e32 v99, 0, v99
	v_cvt_pk_f16_f32 v103, v98, v99
	ds_write_b128 v58, v[100:103] offset:288
	v_lshlrev_b32_e32 v92, 16, v72
	v_and_b32_e32 v93, 0xffff0000, v72
	v_lshlrev_b32_e32 v94, 16, v88
	v_and_b32_e32 v95, 0xffff0000, v88
	v_add_f32_e32 v92, v94, v92
	v_add_f32_e32 v93, v95, v93
	v_fma_f32 v94, v10, v37, v18
	v_fma_f32 v95, v11, v37, v19
	v_fmac_f32_e32 v94, v2, v92
	v_fmac_f32_e32 v95, v3, v93
	v_max_f32_e32 v94, 0, v94
	v_max_f32_e32 v95, 0, v95
	v_cvt_pk_f16_f32 v104, v94, v95
	v_lshlrev_b32_e32 v96, 16, v73
	v_and_b32_e32 v97, 0xffff0000, v73
	v_lshlrev_b32_e32 v98, 16, v89
	v_and_b32_e32 v99, 0xffff0000, v89
	v_add_f32_e32 v96, v98, v96
	v_add_f32_e32 v97, v99, v97
	v_fma_f32 v98, v12, v37, v20
	v_fma_f32 v99, v13, v37, v21
	v_fmac_f32_e32 v98, v4, v96
	v_fmac_f32_e32 v99, v5, v97
	v_max_f32_e32 v98, 0, v98
	v_max_f32_e32 v99, 0, v99
	v_cvt_pk_f16_f32 v105, v98, v99
	v_lshlrev_b32_e32 v92, 16, v74
	v_and_b32_e32 v93, 0xffff0000, v74
	v_lshlrev_b32_e32 v94, 16, v90
	v_and_b32_e32 v95, 0xffff0000, v90
	v_add_f32_e32 v92, v94, v92
	v_add_f32_e32 v93, v95, v93
	v_fma_f32 v94, v14, v37, v22
	v_fma_f32 v95, v15, v37, v23
	v_fmac_f32_e32 v94, v6, v92
	v_fmac_f32_e32 v95, v7, v93
	v_max_f32_e32 v94, 0, v94
	v_max_f32_e32 v95, 0, v95
	v_cvt_pk_f16_f32 v106, v94, v95
	v_lshlrev_b32_e32 v96, 16, v75
	v_and_b32_e32 v97, 0xffff0000, v75
	v_lshlrev_b32_e32 v98, 16, v91
	v_and_b32_e32 v99, 0xffff0000, v91
	v_add_f32_e32 v96, v98, v96
	v_add_f32_e32 v97, v99, v97
	v_fma_f32 v98, v16, v37, v24
	v_fma_f32 v99, v17, v37, v25
	v_fmac_f32_e32 v98, v8, v96
	v_fmac_f32_e32 v99, v9, v97
	v_max_f32_e32 v98, 0, v98
	v_max_f32_e32 v99, 0, v99
	v_cvt_pk_f16_f32 v107, v98, v99
	ds_write_b128 v58, v[104:107] offset:432
	s_waitcnt vmcnt(0)
	v_lshl_or_b32 v42, v30, 7, v54
	v_lshl_or_b32 v46, v26, 7, v54
	v_lshl_or_b32 v43, v31, 7, v54
	v_lshl_or_b32 v47, v27, 7, v54
	v_lshl_or_b32 v44, v32, 7, v54
	v_lshl_or_b32 v48, v28, 7, v54
	v_lshl_or_b32 v45, v33, 7, v54
	v_lshl_or_b32 v49, v29, 7, v54
	global_load_dwordx4 v[60:63], v42, s[10:11]
	global_load_dwordx4 v[76:79], v46, s[14:15]
	global_load_dwordx4 v[64:67], v43, s[10:11]
	global_load_dwordx4 v[80:83], v47, s[14:15]
	global_load_dwordx4 v[68:71], v44, s[10:11]
	global_load_dwordx4 v[84:87], v48, s[14:15]
	global_load_dwordx4 v[72:75], v45, s[10:11]
	global_load_dwordx4 v[88:91], v49, s[14:15]
	v_mov_b32_e32 v34, v38
	v_mov_b32_e32 v35, v39
	v_mov_b32_e32 v36, v40
	v_mov_b32_e32 v37, v41
	s_min_u32 s23, s20, s22
	v_add_u32_e32 v55, s23, v56
	s_add_i32 s20, s20, 0x80
	global_load_dwordx4 v[26:29], v55, s[4:5]
	global_load_dwordx4 v[30:33], v55, s[6:7]
	global_load_dwordx4 v[38:41], v55, s[8:9]
	s_waitcnt lgkmcnt(0)
	ds_read_b128 v[92:95], v59
	ds_read_b128 v[96:99], v59 offset:16
	ds_read_b128 v[100:103], v59 offset:32
	ds_read_b128 v[104:107], v59 offset:48
	ds_read_b128 v[42:45], v57
	ds_read_b128 v[46:49], v57 offset:1024
	ds_read_b128 v[124:127], v57 offset:2048
	s_waitcnt lgkmcnt(2)
	v_mfma_f32_32x32x16_f16 v[108:123], v[92:95], v[42:45], 0
	ds_read_b128 v[42:45], v57 offset:3072
	s_waitcnt lgkmcnt(2)
	v_mfma_f32_32x32x16_f16 v[108:123], v[96:99], v[46:49], v[108:123]
	ds_read_b128 v[46:49], v57 offset:4096
	s_waitcnt lgkmcnt(2)
	v_mfma_f32_32x32x16_f16 v[108:123], v[100:103], v[124:127], v[108:123]
	ds_read_b128 v[124:127], v57 offset:5120
	s_waitcnt lgkmcnt(2)
	v_mfma_f32_32x32x16_f16 v[108:123], v[104:107], v[42:45], v[108:123]
	ds_read_b128 v[42:45], v57 offset:6144
	s_nop 11
	v_add_f32_e32 v52, v108, v52
	v_fmac_f32_e32 v50, v108, v108
	v_add_f32_e32 v52, v109, v52
	v_fmac_f32_e32 v50, v109, v109
	v_add_f32_e32 v52, v110, v52
	v_fmac_f32_e32 v50, v110, v110
	v_add_f32_e32 v52, v111, v52
	v_fmac_f32_e32 v50, v111, v111
	v_add_f32_e32 v52, v112, v52
	v_fmac_f32_e32 v50, v112, v112
	v_add_f32_e32 v52, v113, v52
	v_fmac_f32_e32 v50, v113, v113
	v_add_f32_e32 v52, v114, v52
	v_fmac_f32_e32 v50, v114, v114
	v_add_f32_e32 v52, v115, v52
	v_fmac_f32_e32 v50, v115, v115
	v_add_f32_e32 v52, v116, v52
	v_fmac_f32_e32 v50, v116, v116
	v_add_f32_e32 v52, v117, v52
	v_fmac_f32_e32 v50, v117, v117
	v_add_f32_e32 v52, v118, v52
	v_fmac_f32_e32 v50, v118, v118
	v_add_f32_e32 v52, v119, v52
	v_fmac_f32_e32 v50, v119, v119
	v_add_f32_e32 v52, v120, v52
	v_fmac_f32_e32 v50, v120, v120
	v_add_f32_e32 v52, v121, v52
	v_fmac_f32_e32 v50, v121, v121
	v_add_f32_e32 v52, v122, v52
	v_fmac_f32_e32 v50, v122, v122
	v_add_f32_e32 v52, v123, v52
	v_fmac_f32_e32 v50, v123, v123
	s_waitcnt lgkmcnt(2)
	v_mfma_f32_32x32x16_f16 v[108:123], v[92:95], v[46:49], 0
	ds_read_b128 v[46:49], v57 offset:7168
	s_waitcnt lgkmcnt(2)
	v_mfma_f32_32x32x16_f16 v[108:123], v[96:99], v[124:127], v[108:123]
	s_waitcnt lgkmcnt(1)
	v_mfma_f32_32x32x16_f16 v[108:123], v[100:103], v[42:45], v[108:123]
	s_waitcnt lgkmcnt(0)
	v_mfma_f32_32x32x16_f16 v[108:123], v[104:107], v[46:49], v[108:123]
	s_nop 11
	v_add_f32_e32 v53, v108, v53
	v_fmac_f32_e32 v51, v108, v108
	v_add_f32_e32 v53, v109, v53
	v_fmac_f32_e32 v51, v109, v109
	v_add_f32_e32 v53, v110, v53
	v_fmac_f32_e32 v51, v110, v110
	v_add_f32_e32 v53, v111, v53
	v_fmac_f32_e32 v51, v111, v111
	v_add_f32_e32 v53, v112, v53
	v_fmac_f32_e32 v51, v112, v112
	v_add_f32_e32 v53, v113, v53
	v_fmac_f32_e32 v51, v113, v113
	v_add_f32_e32 v53, v114, v53
	v_fmac_f32_e32 v51, v114, v114
	v_add_f32_e32 v53, v115, v53
	v_fmac_f32_e32 v51, v115, v115
	v_add_f32_e32 v53, v116, v53
	v_fmac_f32_e32 v51, v116, v116
	v_add_f32_e32 v53, v117, v53
	v_fmac_f32_e32 v51, v117, v117
	v_add_f32_e32 v53, v118, v53
	v_fmac_f32_e32 v51, v118, v118
	v_add_f32_e32 v53, v119, v53
	v_fmac_f32_e32 v51, v119, v119
	v_add_f32_e32 v53, v120, v53
	v_fmac_f32_e32 v51, v120, v120
	v_add_f32_e32 v53, v121, v53
	v_fmac_f32_e32 v51, v121, v121
	v_add_f32_e32 v53, v122, v53
	v_fmac_f32_e32 v51, v122, v122
	v_add_f32_e32 v53, v123, v53
	v_fmac_f32_e32 v51, v123, v123
	s_add_i32 s16, s16, -1
	s_cmp_lg_u32 s16, 0
	s_cbranch_scc1 .Lpl_loop
	s_branch .LBB7_14
